# attention PV loop: transposed V reads of the next step issued before the current step's MFMAs (static V image), two alternating fragment register sets
# baseline (speedup 1.0000x reference)
.Latt_b3m:
	s_waitcnt vmcnt(12)
	s_barrier
	ds_read_b64_tr_b16 v[228:229], v195
	ds_read_b64_tr_b16 v[230:231], v195 offset:1024
	ds_read_b64_tr_b16 v[232:233], v196
	ds_read_b64_tr_b16 v[234:235], v196 offset:1024
	s_waitcnt lgkmcnt(0)
	ds_read_b64_tr_b16 v[236:237], v197
	ds_read_b64_tr_b16 v[238:239], v197 offset:1024
	ds_read_b64_tr_b16 v[240:241], v198
	ds_read_b64_tr_b16 v[242:243], v198 offset:1024
	s_nop 0
	v_add_f32_e32 v34, v48, v14
	v_mfma_f32_32x32x16_bf16 v[18:33], v[228:231], v[2:5], 0
	v_exp_f32_e32 v63, v94
	v_exp_f32_e32 v65, v95
	v_exp_f32_e32 v64, v96
	v_mfma_f32_32x32x16_bf16 v[2:17], v[232:235], v[2:5], 0
	v_exp_f32_e32 v70, v70
	v_add_f32_e32 v34, v63, v34
	v_cvt_pk_bf16_f32 v82, v119, v120
	v_cvt_pk_bf16_f32 v83, v121, v122
	v_cvt_pk_bf16_f32 v84, v123, v124
	v_cvt_pk_bf16_f32 v85, v125, v126
	s_waitcnt lgkmcnt(0)
	ds_read_b64_tr_b16 v[228:229], v199
	ds_read_b64_tr_b16 v[230:231], v199 offset:1024
	ds_read_b64_tr_b16 v[232:233], v200
	ds_read_b64_tr_b16 v[234:235], v200 offset:1024
	v_add_f32_e32 v34, v65, v34
	v_mfma_f32_32x32x16_bf16 v[18:33], v[236:239], v[82:85], v[18:33]
	v_add_f32_e32 v34, v64, v34
	v_add_f32_e32 v59, v70, v34
	ds_bpermute_b32 v60, v118, v59
	v_mfma_f32_32x32x16_bf16 v[2:17], v[240:243], v[82:85], v[2:17]
	s_and_b64 vcc, exec, s[72:73]
	s_mov_b64 s[4:5], -1
	s_cbranch_vccnz .LBB0_473
	s_lshl_b32 s90, s37, 1
	s_nop 0
	s_add_i32 m0, s75, 0x800
	s_nop 0
	s_mov_b64 s[4:5], 0

.LBB0_475:
	s_nop 0
	v_cvt_pk_bf16_f32 v82, v103, v106
	v_cvt_pk_bf16_f32 v83, v107, v110
	v_cvt_pk_bf16_f32 v84, v111, v114
	v_cvt_pk_bf16_f32 v85, v115, v117
	s_waitcnt lgkmcnt(0)
	ds_read_b64_tr_b16 v[236:237], v201
	ds_read_b64_tr_b16 v[238:239], v201 offset:1024
	ds_read_b64_tr_b16 v[240:241], v202
	ds_read_b64_tr_b16 v[242:243], v202 offset:1024
	s_nop 0
	v_mfma_f32_32x32x16_bf16 v[18:33], v[228:231], v[82:85], v[18:33]
	v_mfma_f32_32x32x16_bf16 v[2:17], v[232:235], v[82:85], v[2:17]
	v_cvt_pk_bf16_f32 v82, v102, v104
	v_cvt_pk_bf16_f32 v83, v105, v108
	v_cvt_pk_bf16_f32 v84, v109, v112
	v_cvt_pk_bf16_f32 v85, v113, v116
	s_waitcnt lgkmcnt(0)
	ds_read_b64_tr_b16 v[228:229], v195 offset:8192
	ds_read_b64_tr_b16 v[230:231], v195 offset:9216
	ds_read_b64_tr_b16 v[232:233], v196 offset:8192
	ds_read_b64_tr_b16 v[234:235], v196 offset:9216
	s_nop 0
	v_mfma_f32_32x32x16_bf16 v[18:33], v[236:239], v[82:85], v[18:33]
	v_mfma_f32_32x32x16_bf16 v[2:17], v[240:243], v[82:85], v[2:17]
	s_and_b64 vcc, exec, s[72:73]
	s_mov_b64 s[4:5], -1
	s_cbranch_vccnz .LBB0_477
	s_lshl_b32 s90, s37, 1
	s_nop 0
	s_nop 0
	s_mov_b64 s[4:5], 0

.LBB0_479:
	s_nop 0
	v_cvt_pk_bf16_f32 v82, v72, v75
	v_cvt_pk_bf16_f32 v83, v76, v79
	v_cvt_pk_bf16_f32 v84, v80, v98
	v_cvt_pk_bf16_f32 v85, v99, v101
	s_waitcnt lgkmcnt(0)
	ds_read_b64_tr_b16 v[236:237], v197 offset:8192
	ds_read_b64_tr_b16 v[238:239], v197 offset:9216
	ds_read_b64_tr_b16 v[240:241], v198 offset:8192
	ds_read_b64_tr_b16 v[242:243], v198 offset:9216
	v_cvt_pk_bf16_f32 v72, v71, v73
	v_cvt_pk_bf16_f32 v73, v74, v77
	v_cvt_pk_bf16_f32 v74, v78, v81
	v_cvt_pk_bf16_f32 v75, v97, v100
	s_nop 0
	v_mfma_f32_32x32x16_bf16 v[18:33], v[228:231], v[82:85], v[18:33]
	v_mfma_f32_32x32x16_bf16 v[2:17], v[232:235], v[82:85], v[2:17]
	s_waitcnt lgkmcnt(0)
	ds_read_b64_tr_b16 v[228:229], v199 offset:8192
	ds_read_b64_tr_b16 v[230:231], v199 offset:9216
	ds_read_b64_tr_b16 v[232:233], v200 offset:8192
	ds_read_b64_tr_b16 v[234:235], v200 offset:9216
	s_nop 0
	v_mfma_f32_32x32x16_bf16 v[18:33], v[236:239], v[72:75], v[18:33]
	v_mfma_f32_32x32x16_bf16 v[2:17], v[240:243], v[72:75], v[2:17]
	s_and_b64 vcc, exec, s[72:73]
	s_mov_b64 s[4:5], -1
	s_cbranch_vccnz .LBB0_481
	v_mov_b32_e32 v71, v0
	s_lshl_b32 s90, s37, 1
	v_bfe_u32 v76, v71, 3, 3
	s_add_i32 m0, s75, 0x800
	v_or_b32_e32 v71, s20, v76
	v_mul_lo_u32 v71, v71, s81
	v_add_u32_e32 v71, s82, v71
	v_max_i32_e32 v71, 0, v71
	s_mov_b64 s[4:5], 0

.LBB0_483:
	s_mov_b32 m0, s27
	s_andn2_b64 vcc, exec, s[96:97]
	v_cvt_pk_bf16_f32 v72, v41, v46
	v_cvt_pk_bf16_f32 v73, v47, v53
	v_cvt_pk_bf16_f32 v74, v54, v67
	v_cvt_pk_bf16_f32 v75, v68, v69
	s_waitcnt lgkmcnt(0)
	ds_read_b64_tr_b16 v[236:237], v201 offset:8192
	ds_read_b64_tr_b16 v[238:239], v201 offset:9216
	ds_read_b64_tr_b16 v[240:241], v202 offset:8192
	ds_read_b64_tr_b16 v[242:243], v202 offset:9216
	v_cvt_pk_bf16_f32 v44, v38, v44
	v_cvt_pk_bf16_f32 v45, v45, v51
	v_cvt_pk_bf16_f32 v46, v52, v57
	v_cvt_pk_bf16_f32 v47, v58, v62
	s_nop 0
	v_mfma_f32_32x32x16_bf16 v[18:33], v[228:231], v[72:75], v[18:33]
	v_mfma_f32_32x32x16_bf16 v[2:17], v[232:235], v[72:75], v[2:17]
	s_waitcnt lgkmcnt(0)
	ds_read_b64_tr_b16 v[228:229], v195 offset:16384
	ds_read_b64_tr_b16 v[230:231], v195 offset:17408
	ds_read_b64_tr_b16 v[232:233], v196 offset:16384
	ds_read_b64_tr_b16 v[234:235], v196 offset:17408
	v_cvt_pk_bf16_f32 v42, v37, v42
	v_cvt_pk_bf16_f32 v43, v43, v49
	s_nop 0
	v_mfma_f32_32x32x16_bf16 v[18:33], v[236:239], v[44:47], v[18:33]
	v_mfma_f32_32x32x16_bf16 v[2:17], v[240:243], v[44:47], v[2:17]
	v_cvt_pk_bf16_f32 v44, v50, v55
	v_cvt_pk_bf16_f32 v45, v56, v61
	s_waitcnt lgkmcnt(0)
	ds_read_b64_tr_b16 v[236:237], v197 offset:16384
	ds_read_b64_tr_b16 v[238:239], v197 offset:17408
	ds_read_b64_tr_b16 v[240:241], v198 offset:16384
	ds_read_b64_tr_b16 v[242:243], v198 offset:17408
	v_cvt_pk_bf16_f32 v34, v36, v39
	v_cvt_pk_bf16_f32 v35, v40, v48
	v_cvt_pk_bf16_f32 v36, v63, v65
	v_cvt_pk_bf16_f32 v37, v64, v70
	s_nop 0
	v_mfma_f32_32x32x16_bf16 v[18:33], v[228:231], v[42:45], v[18:33]
	v_mfma_f32_32x32x16_bf16 v[2:17], v[232:235], v[42:45], v[2:17]
	s_waitcnt lgkmcnt(0)
	s_nop 0
	v_mfma_f32_32x32x16_bf16 v[18:33], v[236:239], v[34:37], v[18:33]
	v_cndmask_b32_e64 v42, 0, 1, s[96:97]
	v_cmp_ne_u32_e64 s[72:73], 1, v42
	v_mfma_f32_32x32x16_bf16 v[2:17], v[240:243], v[34:37], v[2:17]
	s_cbranch_vccnz .LBB0_485
	s_waitcnt vmcnt(0)
